# speedup vs baseline: 1.0045x; 1.0045x over previous
.LBB3_9:
	ds_read_b128 v[2:5], v89
	ds_read_b128 v[22:25], v89 offset:1024
	s_xor_b64 s[6:7], s[6:7], -1
	s_andn2_b64 vcc, exec, s[6:7]
	s_waitcnt lgkmcnt(1)
	v_mfma_f32_32x32x16_f16 v[2:17], v[2:5], v[72:75], 0
	s_waitcnt lgkmcnt(0)
	v_mfma_f32_32x32x16_f16 v[2:17], v[22:25], v[76:79], v[2:17]
	ds_read_b128 v[22:25], v89 offset:4096
	ds_read_b128 v[106:109], v89 offset:5120
	ds_read_b128 v[110:113], v89 offset:2048
	ds_read_b128 v[114:117], v89 offset:6144
	ds_read_b128 v[118:121], v89 offset:3072
	s_waitcnt lgkmcnt(4)
	v_mfma_f32_32x32x16_f16 v[24:39], v[22:25], v[72:75], 0
	s_waitcnt lgkmcnt(3)
	v_mfma_f32_32x32x16_f16 v[24:39], v[106:109], v[76:79], v[24:39]
	s_waitcnt lgkmcnt(2)
	v_mfma_f32_32x32x16_f16 v[2:17], v[110:113], v[80:83], v[2:17]
	s_waitcnt lgkmcnt(1)
	v_mfma_f32_32x32x16_f16 v[24:39], v[114:117], v[80:83], v[24:39]
	s_nop 9
	v_exp_f32_e32 v2, v2
	v_exp_f32_e32 v22, v3
	v_exp_f32_e32 v3, v4
	v_exp_f32_e32 v23, v5
	v_exp_f32_e32 v4, v6
	v_exp_f32_e32 v6, v7
	v_exp_f32_e32 v5, v8
	v_exp_f32_e32 v7, v9
	v_exp_f32_e32 v10, v10
	v_exp_f32_e32 v11, v11
	v_exp_f32_e32 v12, v12
	v_exp_f32_e32 v13, v13
	v_exp_f32_e32 v8, v14
	v_exp_f32_e32 v14, v15
	v_exp_f32_e32 v9, v16
	v_exp_f32_e32 v15, v17
	v_cvt_pk_bf16_f32 v5, v5, v7
	v_cvt_pk_bf16_f32 v4, v4, v6
	v_cvt_pk_bf16_f32 v3, v3, v23
	v_cvt_pk_bf16_f32 v2, v2, v22
	v_cvt_pk_bf16_f32 v9, v9, v15
	v_cvt_pk_bf16_f32 v8, v8, v14
	v_cvt_pk_bf16_f32 v7, v12, v13
	v_cvt_pk_bf16_f32 v6, v10, v11
	s_nop 1
	v_permlane16_swap_b32_e32 v2, v6
	v_permlane16_swap_b32_e32 v3, v7
	v_permlane16_swap_b32_e32 v4, v8
	v_permlane16_swap_b32_e32 v5, v9
	v_exp_f32_e32 v114, v24
	v_exp_f32_e32 v22, v26
	v_exp_f32_e32 v23, v28
	v_exp_f32_e32 v24, v30
	s_waitcnt lgkmcnt(0)
	v_mfma_f32_16x16x32_bf16 v[6:9], v[118:121], v[6:9], v[18:21]
	ds_read_b128 v[10:13], v89 offset:7168
	ds_read_b128 v[14:17], v89 offset:8192
	ds_read_b128 v[106:109], v89 offset:9216
	ds_read_b128 v[110:113], v89 offset:10240
	v_exp_f32_e32 v18, v31
	v_exp_f32_e32 v19, v29
	v_exp_f32_e32 v20, v27
	v_mfma_f32_16x16x32_bf16 v[2:5], v[118:121], v[2:5], v[84:87]
	s_nop 2
	v_exp_f32_e32 v84, v25
	v_cvt_pk_bf16_f32 v87, v24, v18
	v_cvt_pk_bf16_f32 v86, v23, v19
	v_cvt_pk_bf16_f32 v85, v22, v20
	s_waitcnt lgkmcnt(2)
	v_mfma_f32_32x32x16_f16 v[16:31], v[14:17], v[72:75], 0
	v_exp_f32_e32 v14, v32
	v_exp_f32_e32 v15, v34
	v_exp_f32_e32 v32, v36
	v_exp_f32_e32 v34, v37
	v_exp_f32_e32 v36, v38
	v_exp_f32_e32 v37, v39
	v_exp_f32_e32 v38, v35
	s_waitcnt lgkmcnt(1)
	v_mfma_f32_32x32x16_f16 v[16:31], v[106:109], v[76:79], v[16:31]
	v_exp_f32_e32 v39, v33
	v_cvt_pk_bf16_f32 v84, v114, v84
	v_cvt_pk_bf16_f32 v35, v36, v37
	v_cvt_pk_bf16_f32 v34, v32, v34
	v_cvt_pk_bf16_f32 v33, v15, v38
	v_cvt_pk_bf16_f32 v32, v14, v39
	s_nop 1
	v_permlane16_swap_b32_e32 v84, v32
	v_permlane16_swap_b32_e32 v85, v33
	v_permlane16_swap_b32_e32 v86, v34
	v_permlane16_swap_b32_e32 v87, v35
	ds_read_b128 v[36:39], v89 offset:11264
	s_nop 0
	v_mfma_f32_16x16x32_bf16 v[84:87], v[10:13], v[84:87], v[2:5]
	s_nop 2
	ds_read_b128 v[2:5], v89 offset:12288
	s_waitcnt lgkmcnt(2)
	v_mfma_f32_32x32x16_f16 v[16:31], v[110:113], v[80:83], v[16:31]
	v_mfma_f32_16x16x32_bf16 v[106:109], v[10:13], v[32:35], v[6:9]
	s_nop 10
	v_exp_f32_e32 v114, v16
	v_exp_f32_e32 v118, v17
	v_exp_f32_e32 v18, v18
	s_waitcnt lgkmcnt(0)
	v_mfma_f32_32x32x16_f16 v[2:17], v[2:5], v[72:75], 0
	v_exp_f32_e32 v20, v20
	v_exp_f32_e32 v21, v21
	v_exp_f32_e32 v19, v19
	ds_read_b128 v[32:35], v89 offset:13312
	ds_read_b128 v[110:113], v89 offset:14336
	v_cvt_pk_bf16_f32 v114, v114, v118
	v_cvt_pk_bf16_f32 v116, v20, v21
	v_cvt_pk_bf16_f32 v115, v18, v19
	ds_read_b128 v[118:121], v89 offset:15360
	ds_read_b128 v[18:21], v89 offset:16384
	v_exp_f32_e32 v22, v22
	v_exp_f32_e32 v23, v23
	s_waitcnt lgkmcnt(3)
	v_mfma_f32_32x32x16_f16 v[2:17], v[32:35], v[76:79], v[2:17]
	v_exp_f32_e32 v29, v29
	v_exp_f32_e32 v27, v27
	v_cvt_pk_bf16_f32 v117, v22, v23
	v_exp_f32_e32 v22, v24
	v_exp_f32_e32 v23, v26
	v_exp_f32_e32 v24, v28
	v_exp_f32_e32 v26, v30
	v_exp_f32_e32 v28, v31
	v_exp_f32_e32 v25, v25
	ds_read_b128 v[122:125], v89 offset:17408
	s_waitcnt lgkmcnt(3)
	v_mfma_f32_32x32x16_f16 v[2:17], v[110:113], v[80:83], v[2:17]
	v_cvt_pk_bf16_f32 v113, v26, v28
	v_cvt_pk_bf16_f32 v112, v24, v29
	v_cvt_pk_bf16_f32 v111, v23, v27
	v_cvt_pk_bf16_f32 v110, v22, v25
	s_nop 1
	v_permlane16_swap_b32_e32 v114, v110
	v_permlane16_swap_b32_e32 v115, v111
	s_waitcnt lgkmcnt(1)
	v_mfma_f32_32x32x16_f16 v[18:33], v[18:21], v[72:75], 0
	v_permlane16_swap_b32_e32 v116, v112
	v_permlane16_swap_b32_e32 v117, v113
	v_exp_f32_e32 v2, v2
	v_exp_f32_e32 v4, v4
	v_exp_f32_e32 v5, v5
	v_mfma_f32_16x16x32_bf16 v[84:87], v[36:39], v[114:117], v[84:87]
	v_exp_f32_e32 v3, v3
	v_exp_f32_e32 v6, v6
	v_exp_f32_e32 v7, v7
	v_mfma_f32_16x16x32_bf16 v[34:37], v[36:39], v[110:113], v[106:109]
	ds_read_b128 v[110:113], v89 offset:19456
	v_exp_f32_e32 v8, v8
	v_exp_f32_e32 v9, v9
	ds_read_b128 v[106:109], v89 offset:18432
	s_waitcnt lgkmcnt(2)
	v_mfma_f32_32x32x16_f16 v[18:33], v[122:125], v[76:79], v[18:33]
	v_exp_f32_e32 v13, v13
	v_exp_f32_e32 v11, v11
	ds_read_b128 v[122:125], v89 offset:21504
	s_waitcnt lgkmcnt(1)
	v_mfma_f32_32x32x16_f16 v[18:33], v[106:109], v[80:83], v[18:33]
	v_cvt_pk_bf16_f32 v107, v4, v5
	v_cvt_pk_bf16_f32 v106, v2, v3
	ds_read_b128 v[2:5], v89 offset:20480
	v_cvt_pk_bf16_f32 v109, v8, v9
	v_cvt_pk_bf16_f32 v108, v6, v7
	v_exp_f32_e32 v6, v10
	v_exp_f32_e32 v7, v12
	v_exp_f32_e32 v8, v14
	v_exp_f32_e32 v9, v16
	v_exp_f32_e32 v10, v17
	v_exp_f32_e32 v12, v15
	v_cvt_pk_bf16_f32 v115, v7, v13
	v_cvt_pk_bf16_f32 v114, v6, v11
	v_cvt_pk_bf16_f32 v117, v9, v10
	v_cvt_pk_bf16_f32 v116, v8, v12
	s_waitcnt lgkmcnt(0)
	v_mfma_f32_32x32x16_f16 v[2:17], v[2:5], v[72:75], 0
	v_permlane16_swap_b32_e32 v106, v114
	v_permlane16_swap_b32_e32 v107, v115
	v_permlane16_swap_b32_e32 v108, v116
	v_permlane16_swap_b32_e32 v109, v117
	v_mfma_f32_32x32x16_f16 v[2:17], v[122:125], v[76:79], v[2:17]
	v_exp_f32_e32 v18, v18
	v_exp_f32_e32 v20, v20
	v_exp_f32_e32 v21, v21
	v_exp_f32_e32 v19, v19
	v_exp_f32_e32 v22, v22
	v_exp_f32_e32 v24, v24
	v_exp_f32_e32 v25, v25
	v_mfma_f32_16x16x32_bf16 v[84:87], v[118:121], v[106:109], v[84:87]
	v_exp_f32_e32 v23, v23
	v_exp_f32_e32 v29, v29
	v_exp_f32_e32 v27, v27
	v_mfma_f32_16x16x32_bf16 v[34:37], v[118:121], v[114:117], v[34:37]
	ds_read_b128 v[106:109], v89 offset:22528
	ds_read_b128 v[114:117], v89 offset:23552
	ds_read_b128 v[122:125], v89 offset:25600
	s_waitcnt lgkmcnt(2)
	v_mfma_f32_32x32x16_f16 v[2:17], v[106:109], v[80:83], v[2:17]
	v_cvt_pk_bf16_f32 v107, v20, v21
	v_cvt_pk_bf16_f32 v106, v18, v19
	ds_read_b128 v[18:21], v89 offset:24576
	v_cvt_pk_bf16_f32 v109, v24, v25
	v_cvt_pk_bf16_f32 v108, v22, v23
	v_exp_f32_e32 v22, v26
	v_exp_f32_e32 v23, v28
	v_exp_f32_e32 v24, v30
	v_exp_f32_e32 v25, v32
	v_exp_f32_e32 v26, v33
	v_exp_f32_e32 v28, v31
	v_cvt_pk_bf16_f32 v119, v23, v29
	v_cvt_pk_bf16_f32 v118, v22, v27
	v_cvt_pk_bf16_f32 v121, v25, v26
	v_cvt_pk_bf16_f32 v120, v24, v28
	s_waitcnt lgkmcnt(0)
	v_mfma_f32_32x32x16_f16 v[18:33], v[18:21], v[72:75], 0
	v_permlane16_swap_b32_e32 v106, v118
	v_permlane16_swap_b32_e32 v107, v119
	v_permlane16_swap_b32_e32 v108, v120
	v_permlane16_swap_b32_e32 v109, v121
	v_mfma_f32_32x32x16_f16 v[18:33], v[122:125], v[76:79], v[18:33]
	v_exp_f32_e32 v2, v2
	v_exp_f32_e32 v4, v4
	v_exp_f32_e32 v5, v5
	v_exp_f32_e32 v3, v3
	v_exp_f32_e32 v6, v6
	v_exp_f32_e32 v8, v8
	v_exp_f32_e32 v9, v9
	v_mfma_f32_16x16x32_bf16 v[84:87], v[110:113], v[106:109], v[84:87]
	v_exp_f32_e32 v7, v7
	v_exp_f32_e32 v13, v13
	v_exp_f32_e32 v11, v11
	v_mfma_f32_16x16x32_bf16 v[34:37], v[110:113], v[118:121], v[34:37]
	ds_read_b128 v[106:109], v89 offset:26624
	ds_read_b128 v[110:113], v89 offset:27648
	ds_read_b128 v[122:125], v89 offset:29696
	s_waitcnt lgkmcnt(2)
	v_mfma_f32_32x32x16_f16 v[18:33], v[106:109], v[80:83], v[18:33]
	v_cvt_pk_bf16_f32 v107, v4, v5
	v_cvt_pk_bf16_f32 v106, v2, v3
	ds_read_b128 v[2:5], v89 offset:28672
	v_cvt_pk_bf16_f32 v109, v8, v9
	v_cvt_pk_bf16_f32 v108, v6, v7
	v_exp_f32_e32 v6, v10
	v_exp_f32_e32 v7, v12
	v_exp_f32_e32 v8, v14
	v_exp_f32_e32 v9, v16
	v_exp_f32_e32 v10, v17
	v_exp_f32_e32 v12, v15
	v_cvt_pk_bf16_f32 v119, v7, v13
	v_cvt_pk_bf16_f32 v118, v6, v11
	v_cvt_pk_bf16_f32 v121, v9, v10
	v_cvt_pk_bf16_f32 v120, v8, v12
	s_waitcnt lgkmcnt(0)
	v_mfma_f32_32x32x16_f16 v[2:17], v[2:5], v[72:75], 0
	v_permlane16_swap_b32_e32 v106, v118
	v_permlane16_swap_b32_e32 v107, v119
	v_permlane16_swap_b32_e32 v108, v120
	v_permlane16_swap_b32_e32 v109, v121
	v_mfma_f32_32x32x16_f16 v[2:17], v[122:125], v[76:79], v[2:17]
	v_exp_f32_e32 v38, v20
	v_exp_f32_e32 v20, v22
	v_exp_f32_e32 v22, v24
	v_exp_f32_e32 v24, v25
	v_exp_f32_e32 v25, v21
	v_exp_f32_e32 v23, v23
	v_exp_f32_e32 v39, v19
	v_mfma_f32_16x16x32_bf16 v[84:87], v[114:117], v[106:109], v[84:87]
	v_cvt_pk_bf16_f32 v21, v22, v24
	v_cvt_pk_bf16_f32 v19, v38, v25
	v_exp_f32_e32 v22, v26
	v_mfma_f32_16x16x32_bf16 v[34:37], v[114:117], v[118:121], v[34:37]
	ds_read_b128 v[106:109], v89 offset:30720
	ds_read_b128 v[114:117], v89 offset:31744
	v_exp_f32_e32 v25, v32
	v_exp_f32_e32 v26, v33
	s_waitcnt lgkmcnt(1)
	v_mfma_f32_32x32x16_f16 v[2:17], v[106:109], v[80:83], v[2:17]
	v_exp_f32_e32 v18, v18
	v_cvt_pk_bf16_f32 v20, v20, v23
	v_exp_f32_e32 v23, v28
	v_exp_f32_e32 v24, v30
	v_exp_f32_e32 v28, v31
	v_exp_f32_e32 v29, v29
	v_exp_f32_e32 v27, v27
	v_cvt_pk_bf16_f32 v25, v25, v26
	s_nop 3
	v_exp_f32_e32 v26, v4
	v_exp_f32_e32 v4, v6
	v_exp_f32_e32 v6, v8
	v_exp_f32_e32 v8, v9
	v_exp_f32_e32 v7, v7
	v_exp_f32_e32 v9, v5
	v_cvt_pk_bf16_f32 v18, v18, v39
	v_cvt_pk_bf16_f32 v24, v24, v28
	v_cvt_pk_bf16_f32 v23, v23, v29
	v_cvt_pk_bf16_f32 v22, v22, v27
	v_exp_f32_e32 v2, v2
	v_exp_f32_e32 v27, v3
	v_cvt_pk_bf16_f32 v5, v6, v8
	v_cvt_pk_bf16_f32 v4, v4, v7
	v_cvt_pk_bf16_f32 v3, v26, v9
	v_exp_f32_e32 v6, v10
	v_exp_f32_e32 v7, v12
	v_exp_f32_e32 v8, v14
	v_exp_f32_e32 v9, v16
	v_exp_f32_e32 v10, v17
	v_exp_f32_e32 v12, v15
	v_exp_f32_e32 v13, v13
	v_exp_f32_e32 v11, v11
	v_permlane16_swap_b32_e32 v18, v22
	v_permlane16_swap_b32_e32 v19, v23
	v_permlane16_swap_b32_e32 v20, v24
	v_permlane16_swap_b32_e32 v21, v25
	v_cvt_pk_bf16_f32 v2, v2, v27
	s_nop 0
	v_mfma_f32_16x16x32_bf16 v[18:21], v[110:113], v[18:21], v[84:87]
	v_cvt_pk_bf16_f32 v9, v9, v10
	v_cvt_pk_bf16_f32 v8, v8, v12
	v_cvt_pk_bf16_f32 v7, v7, v13
	v_mfma_f32_16x16x32_bf16 v[22:25], v[110:113], v[22:25], v[34:37]
	v_cvt_pk_bf16_f32 v6, v6, v11
	s_nop 1
	v_permlane16_swap_b32_e32 v2, v6
	v_permlane16_swap_b32_e32 v3, v7
	v_permlane16_swap_b32_e32 v4, v8
	v_permlane16_swap_b32_e32 v5, v9
	s_waitcnt lgkmcnt(0)
	s_nop 0
	v_mfma_f32_16x16x32_bf16 v[84:87], v[114:117], v[2:5], v[18:21]
	s_barrier
	v_mfma_f32_16x16x32_bf16 v[18:21], v[114:117], v[6:9], v[22:25]
	s_cbranch_vccnz .LBB3_11
	s_waitcnt vmcnt(0)
	ds_write_b128 v88, v[40:43]
	ds_write_b128 v88, v[44:47] offset:8192
	ds_write_b128 v88, v[48:51] offset:16384
	ds_write_b128 v88, v[52:55] offset:24576
